# P0 rope-table loop unrolled x8 with loads issued up front; P9 ln_final_w hoisted out of the row loop (no per-store load+vmcnt0)
# speedup vs baseline: 1.0094x; 1.0094x over previous
; __device__ __forceinline__ void p0_prologue(Ctx& X) {
;     ...
;     for (int idx = gt; idx < T * 128; idx += NGT) {
;         const int t = idx >> 7, i = idx & 127;
;         const double ang = (double)XP_pos(X)[t] * INV_FREQ[i];
;         double rev = ang * 0.15915494309189533577; rev -= floor(rev);
;         const float f = (float)rev;
;         XP_COS(X)[idx] = __builtin_amdgcn_cosf(f); XP_SIN(X)[idx] = __builtin_amdgcn_sinf(f);
;     }
.LBB0_17:
	v_lshl_or_b32 v6, s87, 9, v0
	s_mov_b32 s3, 0x100000
	s_lshl_b32 s2, s92, 9
	v_cmp_gt_i32_e32 vcc, s3, v6
	v_ashrrev_i32_e32 v7, 31, v6
	s_and_saveexec_b64 s[4:5], vcc
	s_cbranch_execz .LBB0_20
	v_and_b32_e32 v2, 0x7f, v0
	v_lshlrev_b32_e32 v2, 3, v2
	s_getpc_b64 s[6:7]
	s_add_u32 s6, s6, INV_FREQ@rel32@lo+4
	s_addc_u32 s7, s7, INV_FREQ@rel32@hi+12
	global_load_dwordx2 v[2:3], v2, s[6:7]
	s_load_dwordx2 s[6:7], s[0:1], 0x8
	v_lshl_add_u64 v[4:5], v[6:7], 2, s[90:91]
	s_mov_b64 s[12:13], 0x2600000
	s_ashr_i32 s3, s2, 31
	s_mov_b32 s16, 0x6dc9c883
	v_lshl_add_u64 v[4:5], v[4:5], 0, s[12:13]
	s_lshl_b64 s[12:13], s[2:3], 2
	s_mov_b64 s[14:15], 0
	s_mov_b32 s17, 0x3fc45f30
	s_mov_b32 s3, 0xfffff
	v_mov_b32_e32 v8, v6
	s_cmpk_lg_i32 s92, 0x100
	s_cbranch_scc1 .LBB0_19
	v_ashrrev_i32_e32 v8, 7, v6
	v_lshlrev_b32_e32 v8, 2, v8
	s_waitcnt lgkmcnt(0)
	global_load_dword v16, v8, s[6:7]
	s_add_u32 s6, s6, 0x1000
	s_addc_u32 s7, s7, 0
	global_load_dword v17, v8, s[6:7]
	s_add_u32 s6, s6, 0x1000
	s_addc_u32 s7, s7, 0
	global_load_dword v18, v8, s[6:7]
	s_add_u32 s6, s6, 0x1000
	s_addc_u32 s7, s7, 0
	global_load_dword v19, v8, s[6:7]
	s_add_u32 s6, s6, 0x1000
	s_addc_u32 s7, s7, 0
	global_load_dword v20, v8, s[6:7]
	s_add_u32 s6, s6, 0x1000
	s_addc_u32 s7, s7, 0
	global_load_dword v21, v8, s[6:7]
	s_add_u32 s6, s6, 0x1000
	s_addc_u32 s7, s7, 0
	global_load_dword v22, v8, s[6:7]
	s_add_u32 s6, s6, 0x1000
	s_addc_u32 s7, s7, 0
	global_load_dword v23, v8, s[6:7]
	v_lshlrev_b32_e32 v9, 2, v6
	s_add_u32 s12, s90, 0x2600000
	s_addc_u32 s13, s91, 0
	s_add_u32 s14, s90, 0x2a00000
	s_addc_u32 s15, s91, 0
	s_waitcnt vmcnt(7)
	v_cvt_f64_i32_e32 v[10:11], v16
	v_mul_f64 v[10:11], v[2:3], v[10:11]
	v_mul_f64 v[12:13], v[10:11], s[16:17]
	v_floor_f64_e32 v[12:13], v[12:13]
	v_fma_f64 v[10:11], v[10:11], s[16:17], -v[12:13]
	v_cvt_f32_f64_e32 v14, v[10:11]
	v_cos_f32_e32 v24, v14
	v_sin_f32_e32 v32, v14
	global_store_dword v9, v24, s[12:13]
	global_store_dword v9, v32, s[14:15]
	s_add_u32 s12, s12, 0x80000
	s_addc_u32 s13, s13, 0
	s_add_u32 s14, s14, 0x80000
	s_addc_u32 s15, s15, 0
	s_waitcnt vmcnt(8)
	v_cvt_f64_i32_e32 v[10:11], v17
	v_mul_f64 v[10:11], v[2:3], v[10:11]
	v_mul_f64 v[12:13], v[10:11], s[16:17]
	v_floor_f64_e32 v[12:13], v[12:13]
	v_fma_f64 v[10:11], v[10:11], s[16:17], -v[12:13]
	v_cvt_f32_f64_e32 v14, v[10:11]
	v_cos_f32_e32 v25, v14
	v_sin_f32_e32 v33, v14
	global_store_dword v9, v25, s[12:13]
	global_store_dword v9, v33, s[14:15]
	s_add_u32 s12, s12, 0x80000
	s_addc_u32 s13, s13, 0
	s_add_u32 s14, s14, 0x80000
	s_addc_u32 s15, s15, 0
	s_waitcnt vmcnt(9)
	v_cvt_f64_i32_e32 v[10:11], v18
	v_mul_f64 v[10:11], v[2:3], v[10:11]
	v_mul_f64 v[12:13], v[10:11], s[16:17]
	v_floor_f64_e32 v[12:13], v[12:13]
	v_fma_f64 v[10:11], v[10:11], s[16:17], -v[12:13]
	v_cvt_f32_f64_e32 v14, v[10:11]
	v_cos_f32_e32 v26, v14
	v_sin_f32_e32 v34, v14
	global_store_dword v9, v26, s[12:13]
	global_store_dword v9, v34, s[14:15]
	s_add_u32 s12, s12, 0x80000
	s_addc_u32 s13, s13, 0
	s_add_u32 s14, s14, 0x80000
	s_addc_u32 s15, s15, 0
	s_waitcnt vmcnt(10)
	v_cvt_f64_i32_e32 v[10:11], v19
	v_mul_f64 v[10:11], v[2:3], v[10:11]
	v_mul_f64 v[12:13], v[10:11], s[16:17]
	v_floor_f64_e32 v[12:13], v[12:13]
	v_fma_f64 v[10:11], v[10:11], s[16:17], -v[12:13]
	v_cvt_f32_f64_e32 v14, v[10:11]
	v_cos_f32_e32 v27, v14
	v_sin_f32_e32 v35, v14
	global_store_dword v9, v27, s[12:13]
	global_store_dword v9, v35, s[14:15]
	s_add_u32 s12, s12, 0x80000
	s_addc_u32 s13, s13, 0
	s_add_u32 s14, s14, 0x80000
	s_addc_u32 s15, s15, 0
	s_waitcnt vmcnt(11)
	v_cvt_f64_i32_e32 v[10:11], v20
	v_mul_f64 v[10:11], v[2:3], v[10:11]
	v_mul_f64 v[12:13], v[10:11], s[16:17]
	v_floor_f64_e32 v[12:13], v[12:13]
	v_fma_f64 v[10:11], v[10:11], s[16:17], -v[12:13]
	v_cvt_f32_f64_e32 v14, v[10:11]
	v_cos_f32_e32 v28, v14
	v_sin_f32_e32 v36, v14
	global_store_dword v9, v28, s[12:13]
	global_store_dword v9, v36, s[14:15]
	s_add_u32 s12, s12, 0x80000
	s_addc_u32 s13, s13, 0
	s_add_u32 s14, s14, 0x80000
	s_addc_u32 s15, s15, 0
	s_waitcnt vmcnt(12)
	v_cvt_f64_i32_e32 v[10:11], v21
	v_mul_f64 v[10:11], v[2:3], v[10:11]
	v_mul_f64 v[12:13], v[10:11], s[16:17]
	v_floor_f64_e32 v[12:13], v[12:13]
	v_fma_f64 v[10:11], v[10:11], s[16:17], -v[12:13]
	v_cvt_f32_f64_e32 v14, v[10:11]
	v_cos_f32_e32 v29, v14
	v_sin_f32_e32 v37, v14
	global_store_dword v9, v29, s[12:13]
	global_store_dword v9, v37, s[14:15]
	s_add_u32 s12, s12, 0x80000
	s_addc_u32 s13, s13, 0
	s_add_u32 s14, s14, 0x80000
	s_addc_u32 s15, s15, 0
	s_waitcnt vmcnt(13)
	v_cvt_f64_i32_e32 v[10:11], v22
	v_mul_f64 v[10:11], v[2:3], v[10:11]
	v_mul_f64 v[12:13], v[10:11], s[16:17]
	v_floor_f64_e32 v[12:13], v[12:13]
	v_fma_f64 v[10:11], v[10:11], s[16:17], -v[12:13]
	v_cvt_f32_f64_e32 v14, v[10:11]
	v_cos_f32_e32 v30, v14
	v_sin_f32_e32 v38, v14
	global_store_dword v9, v30, s[12:13]
	global_store_dword v9, v38, s[14:15]
	s_add_u32 s12, s12, 0x80000
	s_addc_u32 s13, s13, 0
	s_add_u32 s14, s14, 0x80000
	s_addc_u32 s15, s15, 0
	s_waitcnt vmcnt(14)
	v_cvt_f64_i32_e32 v[10:11], v23
	v_mul_f64 v[10:11], v[2:3], v[10:11]
	v_mul_f64 v[12:13], v[10:11], s[16:17]
	v_floor_f64_e32 v[12:13], v[12:13]
	v_fma_f64 v[10:11], v[10:11], s[16:17], -v[12:13]
	v_cvt_f32_f64_e32 v14, v[10:11]
	v_cos_f32_e32 v31, v14
	v_sin_f32_e32 v39, v14
	global_store_dword v9, v31, s[12:13]
	global_store_dword v9, v39, s[14:15]
	s_branch .LBB0_20

; #define LAS __attribute__((address_space(3)))
; __device__ __forceinline__ float bf_lo(unsigned u) { return __uint_as_float(u << 16); }
; __device__ __forceinline__ float bf_hi(unsigned u) { return __uint_as_float(u & 0xffff0000u); }
; __device__ __forceinline__ void p9_final(Ctx& X) {
;     const LAS int* tab = (const LAS int*)(X.lds + LDS_TAB);
;     const int gw = X.bid * NWAVES + X.wave, NGW = X.G * NWAVES, lane = X.lane;
;     for (int t = gw; t < T; t += NGW) {
;         const u32x2* hr = (const u32x2*)(XP_Hh(X) + (size_t)t * D) + lane;
;         f32x4 v[8];
; #pragma unroll
;         for (int j = 0; j < 8; ++j) { const u32x2 hv = hr[64 * j]; v[j] = (f32x4){bf_lo(hv.x), bf_hi(hv.x), bf_lo(hv.y), bf_hi(hv.y)}; }
; #pragma unroll
;         for (int k = 0; k < 4; ++k) { const int e = XP_TOPI(X)[t * 4 + k], r = XP_TOPR(X)[t * 4 + k]; const float wk = XP_TOPW(X)[t * 4 + k];
;             const unsigned* yr = (const unsigned*)(XP_YR(X) + ((size_t)tab[8 + e] * 256 + r) * D) + lane;
;     ...
;         f32x4* o = (f32x4*)(X.out + (size_t)t * D) + lane; const f32x4* wr_ = (const f32x4*)XP_ln_final_w(X) + lane;
; #pragma unroll
;         for (int j = 0; j < 8; ++j) { const f32x4 wv = wr_[64 * j]; f32x4 r; r.x = v[j].x * rstd * wv.x; r.y = v[j].y * rstd * wv.y; r.z = v[j].z * rstd * wv.z; r.w = v[j].w * rstd * wv.w; __builtin_nontemporal_store(r, &o[64 * j]); }
.LBB0_1126:
	s_lshl_b32 s2, s87, 3
	s_add_i32 s2, s93, s2
	s_cmpk_gt_i32 s2, 0x1fff
	s_cbranch_scc1 .LBB0_1129
	v_mbcnt_lo_u32_b32 v0, -1, 0
	v_mbcnt_hi_u32_b32 v0, -1, v0
	v_and_b32_e32 v1, 64, v0
	v_add_u32_e32 v1, 64, v1
	v_xor_b32_e32 v2, 1, v0
	v_cmp_lt_i32_e32 vcc, v2, v1
	s_lshl_b32 s4, s92, 3
	s_add_u32 s12, s90, 0x2e00000
	v_cndmask_b32_e32 v2, v0, v2, vcc
	v_lshlrev_b32_e32 v29, 2, v2
	v_xor_b32_e32 v2, 2, v0
	v_cmp_lt_i32_e32 vcc, v2, v1
	s_load_dwordx2 s[6:7], s[0:1], 0x90
	s_addc_u32 s13, s91, 0
	v_cndmask_b32_e32 v2, v0, v2, vcc
	v_lshlrev_b32_e32 v48, 2, v2
	v_xor_b32_e32 v2, 4, v0
	v_cmp_lt_i32_e32 vcc, v2, v1
	s_add_u32 s14, s90, 0x2e20000
	s_addc_u32 s15, s91, 0
	v_cndmask_b32_e32 v2, v0, v2, vcc
	v_lshlrev_b32_e32 v49, 2, v2
	v_xor_b32_e32 v2, 8, v0
	v_cmp_lt_i32_e32 vcc, v2, v1
	v_mov_b32_e32 v5, 0
	s_add_u32 s16, s90, 0x2e40000
	v_cndmask_b32_e32 v2, v0, v2, vcc
	v_lshlrev_b32_e32 v4, 4, v194
	v_lshlrev_b32_e32 v50, 2, v2
	v_xor_b32_e32 v2, 16, v0
	s_addc_u32 s17, s91, 0
	s_waitcnt lgkmcnt(0)
	v_lshl_add_u64 v[6:7], s[6:7], 0, v[4:5]
	s_mov_b64 s[6:7], 0x1400
	v_cmp_lt_i32_e32 vcc, v2, v1
	s_add_u32 s0, s90, 0x26000000
	v_lshl_add_u64 v[10:11], v[6:7], 0, s[6:7]
	s_mov_b64 s[6:7], 0x1800
	v_cndmask_b32_e32 v2, v0, v2, vcc
	s_addc_u32 s1, s91, 0
	v_lshl_add_u64 v[12:13], v[6:7], 0, s[6:7]
	s_mov_b64 s[6:7], 0x1c00
	s_lshl_b32 s3, s87, 5
	s_lshl_b32 s5, s93, 2
	v_lshlrev_b32_e32 v51, 2, v2
	v_xor_b32_e32 v2, 32, v0
	v_lshl_add_u64 v[14:15], v[6:7], 0, s[6:7]
	s_add_i32 s6, s3, s5
	s_ashr_i32 s3, s2, 31
	v_cmp_lt_i32_e32 vcc, v2, v1
	s_lshl_b32 s18, s92, 5
	s_lshl_b64 s[8:9], s[2:3], 12
	v_cndmask_b32_e32 v0, v0, v2, vcc
	s_add_u32 s8, s90, s8
	v_lshlrev_b32_e32 v52, 2, v0
	v_lshlrev_b32_e32 v0, 3, v194
	v_mov_b32_e32 v1, v5
	s_addc_u32 s9, s91, s9
	v_lshl_add_u64 v[0:1], s[8:9], 0, v[0:1]
	s_mov_b64 s[8:9], 0x10000000
	s_ashr_i32 s5, s4, 31
	v_lshl_add_u64 v[16:17], v[0:1], 0, s[8:9]
	s_lshl_b64 s[8:9], s[4:5], 12
	s_lshl_b64 s[20:21], s[2:3], 13
	s_add_u32 s20, s88, s20
	s_addc_u32 s21, s89, s21
	s_mov_b64 s[10:11], 0x1000
	v_lshl_add_u64 v[0:1], s[20:21], 0, v[4:5]
	v_lshl_add_u64 v[8:9], v[6:7], 0, s[10:11]
	v_lshl_add_u64 v[18:19], v[0:1], 0, s[10:11]
	s_lshl_b64 s[10:11], s[4:5], 13
	s_add_i32 s3, 0, 0x22020
	v_lshlrev_b32_e32 v53, 2, v194
	v_mov_b32_e32 v54, 0x358637bd
	s_mov_b32 s5, 0x800000
	global_load_dwordx4 v[196:199], v[6:7], off
	global_load_dwordx4 v[200:203], v[6:7], off offset:1024
	global_load_dwordx4 v[204:207], v[6:7], off offset:2048
	global_load_dwordx4 v[208:211], v[6:7], off offset:3072
	global_load_dwordx4 v[212:215], v[8:9], off
	global_load_dwordx4 v[216:219], v[10:11], off
	global_load_dwordx4 v[220:223], v[12:13], off
	global_load_dwordx4 v[224:227], v[14:15], off
.LBB0_1128:
	s_ashr_i32 s7, s6, 31
	s_lshl_b64 s[20:21], s[6:7], 2
	s_add_u32 s22, s12, s20
	s_addc_u32 s23, s13, s21
	global_load_dwordx2 v[36:37], v[16:17], off
	global_load_dwordx2 v[40:41], v[16:17], off offset:512
	global_load_dwordx2 v[42:43], v[16:17], off offset:1024
	global_load_dwordx2 v[34:35], v[16:17], off offset:1536
	global_load_dwordx2 v[30:31], v[16:17], off offset:2048
	global_load_dwordx2 v[26:27], v[16:17], off offset:2560
	global_load_dwordx2 v[22:23], v[16:17], off offset:3072
	global_load_dwordx2 v[20:21], v[16:17], off offset:3584
	global_load_dwordx4 v[56:59], v5, s[22:23]
	s_add_u32 s22, s14, s20
	s_addc_u32 s23, s15, s21
	s_add_u32 s20, s16, s20
	s_addc_u32 s21, s17, s21
	global_load_dword v64, v5, s[22:23]
	global_load_dword v28, v5, s[20:21]
	s_add_i32 s22, s6, 1
	s_ashr_i32 s23, s22, 31
	s_lshl_b64 s[20:21], s[22:23], 2
	s_add_u32 s22, s14, s20
	s_addc_u32 s23, s15, s21
	global_load_dwordx3 v[60:62], v5, s[22:23]
	s_add_u32 s20, s16, s20
	s_addc_u32 s21, s17, s21
	global_load_dword v4, v5, s[20:21]
	s_add_i32 s22, s6, 2
	s_ashr_i32 s23, s22, 31
	s_lshl_b64 s[20:21], s[22:23], 2
	s_add_u32 s20, s16, s20
	s_addc_u32 s21, s17, s21
	global_load_dwordx2 v[24:25], v5, s[20:21]
	s_add_i32 s2, s2, s4
	s_add_i32 s6, s6, s18
	v_lshl_add_u64 v[16:17], v[16:17], 0, s[8:9]
	s_cmpk_lt_i32 s2, 0x2000
	s_waitcnt vmcnt(0)
	v_lshlrev_b32_e32 v32, 16, v36
	v_and_b32_e32 v33, 0xffff0000, v36
	v_lshlrev_b32_e32 v36, 16, v37
	v_and_b32_e32 v37, 0xffff0000, v37
	v_lshlrev_b32_e32 v38, 16, v40
	v_and_b32_e32 v39, 0xffff0000, v40
	v_lshlrev_b32_e32 v40, 16, v41
	v_and_b32_e32 v41, 0xffff0000, v41
	v_lshlrev_b32_e32 v55, 2, v56
	v_lshlrev_b32_e32 v56, 2, v57
	v_lshlrev_b32_e32 v57, 2, v58
	v_lshlrev_b32_e32 v58, 2, v59
	v_add_u32_e32 v55, s3, v55
	v_add_u32_e32 v59, s3, v56
	v_add_u32_e32 v57, s3, v57
	v_add_u32_e32 v63, s3, v58
	ds_read_b32 v56, v55
	ds_read_b32 v58, v59
	ds_read_b32 v74, v57
	ds_read_b32 v76, v63
	v_ashrrev_i32_e32 v65, 31, v64
	s_waitcnt lgkmcnt(3)
	v_ashrrev_i32_e32 v57, 31, v56
	s_waitcnt lgkmcnt(2)
	v_ashrrev_i32_e32 v59, 31, v58
	s_waitcnt lgkmcnt(1)
	v_ashrrev_i32_e32 v75, 31, v74
	s_waitcnt lgkmcnt(0)
; __device__ __forceinline__ void p9_final(Ctx& X) {
;     ...
;         for (int k = 0; k < 4; ++k) { const int e = XP_TOPI(X)[t * 4 + k], r = XP_TOPR(X)[t * 4 + k]; const float wk = XP_TOPW(X)[t * 4 + k];
;             const unsigned* yr = (const unsigned*)(XP_YR(X) + ((size_t)tab[8 + e] * 256 + r) * D) + lane;
; #pragma unroll
;             for (int j = 0; j < 8; ++j) { const int y = (int)yr[64 * j]; const f32x2 lo = __builtin_amdgcn_cvt_pk_f32_fp8(y, false), hi = __builtin_amdgcn_cvt_pk_f32_fp8(y, true);
;                 v[j].x += wk * lo.x; v[j].y += wk * lo.y; v[j].z += wk * hi.x; v[j].w += wk * hi.y; } }
	v_ashrrev_i32_e32 v77, 31, v76
	v_lshlrev_b64 v[56:57], 19, v[56:57]
	v_lshlrev_b64 v[64:65], 11, v[64:65]
	v_ashrrev_i32_e32 v79, 31, v60
	v_mov_b32_e32 v78, v60
	v_lshlrev_b64 v[58:59], 19, v[58:59]
	v_ashrrev_i32_e32 v81, 31, v61
	v_mov_b32_e32 v80, v61
	v_lshlrev_b64 v[60:61], 19, v[74:75]
	v_ashrrev_i32_e32 v63, 31, v62
	v_lshlrev_b64 v[74:75], 19, v[76:77]
	v_lshl_add_u64 v[56:57], s[0:1], 0, v[56:57]
	v_lshlrev_b64 v[76:77], 11, v[78:79]
	v_lshl_add_u64 v[58:59], s[0:1], 0, v[58:59]
	v_lshlrev_b64 v[78:79], 11, v[80:81]
	v_lshl_add_u64 v[60:61], s[0:1], 0, v[60:61]
	v_lshlrev_b64 v[62:63], 11, v[62:63]
	v_lshl_add_u64 v[74:75], s[0:1], 0, v[74:75]
	v_lshl_add_u64 v[56:57], v[56:57], 0, v[64:65]
	v_lshl_add_u64 v[58:59], v[58:59], 0, v[76:77]
	v_lshl_add_u64 v[60:61], v[60:61], 0, v[78:79]
	v_lshl_add_u64 v[62:63], v[74:75], 0, v[62:63]
	v_readfirstlane_b32 s20, v56
	v_readfirstlane_b32 s21, v57
	v_readfirstlane_b32 s22, v58
	v_readfirstlane_b32 s23, v59
	v_readfirstlane_b32 s24, v60
	v_readfirstlane_b32 s25, v61
	v_readfirstlane_b32 s26, v62
	v_readfirstlane_b32 s27, v63
	global_load_dword v55, v53, s[20:21]
	global_load_dword v62, v53, s[20:21] offset:256
	global_load_dword v74, v53, s[20:21] offset:512
	global_load_dword v78, v53, s[20:21] offset:768
	global_load_dword v82, v53, s[20:21] offset:1024
	global_load_dword v86, v53, s[20:21] offset:1280
	global_load_dword v90, v53, s[20:21] offset:1536
	global_load_dword v94, v53, s[20:21] offset:1792
	global_load_dword v98, v53, s[22:23]
	global_load_dword v102, v53, s[22:23] offset:256
	global_load_dword v106, v53, s[22:23] offset:512
	global_load_dword v110, v53, s[22:23] offset:768
	global_load_dword v114, v53, s[22:23] offset:1024
	global_load_dword v118, v53, s[22:23] offset:1280
	global_load_dword v122, v53, s[22:23] offset:1536
	global_load_dword v126, v53, s[22:23] offset:1792
	global_load_dword v130, v53, s[24:25]
	global_load_dword v134, v53, s[24:25] offset:256
	global_load_dword v138, v53, s[24:25] offset:512
	global_load_dword v142, v53, s[24:25] offset:768
	global_load_dword v146, v53, s[24:25] offset:1024
	global_load_dword v150, v53, s[24:25] offset:1280
	global_load_dword v154, v53, s[24:25] offset:1536
	global_load_dword v158, v53, s[24:25] offset:1792
	global_load_dword v162, v53, s[26:27]
	global_load_dword v166, v53, s[26:27] offset:256
	global_load_dword v170, v53, s[26:27] offset:512
	global_load_dword v174, v53, s[26:27] offset:768
	global_load_dword v178, v53, s[26:27] offset:1024
	global_load_dword v182, v53, s[26:27] offset:1280
	global_load_dword v186, v53, s[26:27] offset:1536
	global_load_dword v190, v53, s[26:27] offset:1792
	v_lshlrev_b32_e32 v44, 16, v42
	v_and_b32_e32 v45, 0xffff0000, v42
	v_lshlrev_b32_e32 v42, 16, v43
	v_and_b32_e32 v43, 0xffff0000, v43
	v_lshlrev_b32_e32 v46, 16, v34
	v_and_b32_e32 v47, 0xffff0000, v34
	v_lshlrev_b32_e32 v34, 16, v35
	v_and_b32_e32 v35, 0xffff0000, v35
	v_lshlrev_b32_e32 v66, 16, v30
	v_and_b32_e32 v67, 0xffff0000, v30
	v_lshlrev_b32_e32 v30, 16, v31
	v_and_b32_e32 v31, 0xffff0000, v31
	v_lshlrev_b32_e32 v68, 16, v26
	v_and_b32_e32 v69, 0xffff0000, v26
	v_lshlrev_b32_e32 v26, 16, v27
	v_and_b32_e32 v27, 0xffff0000, v27
	v_lshlrev_b32_e32 v70, 16, v22
	v_and_b32_e32 v71, 0xffff0000, v22
	v_lshlrev_b32_e32 v22, 16, v23
	v_and_b32_e32 v23, 0xffff0000, v23
	v_lshlrev_b32_e32 v72, 16, v20
	v_and_b32_e32 v73, 0xffff0000, v20
	v_lshlrev_b32_e32 v20, 16, v21
	v_and_b32_e32 v21, 0xffff0000, v21
	s_waitcnt vmcnt(31)
	v_cvt_pk_f32_fp8_e32 v[56:57], v55
	v_cvt_pk_f32_fp8_sdwa v[58:59], v55 src0_sel:WORD_1
	s_waitcnt vmcnt(30)
	v_cvt_pk_f32_fp8_e32 v[60:61], v62
	v_cvt_pk_f32_fp8_sdwa v[62:63], v62 src0_sel:WORD_1
	s_waitcnt vmcnt(29)
	v_cvt_pk_f32_fp8_e32 v[64:65], v74
	v_cvt_pk_f32_fp8_sdwa v[74:75], v74 src0_sel:WORD_1
	s_waitcnt vmcnt(28)
	v_cvt_pk_f32_fp8_e32 v[76:77], v78
	v_cvt_pk_f32_fp8_sdwa v[78:79], v78 src0_sel:WORD_1
	s_waitcnt vmcnt(23)
	v_cvt_pk_f32_fp8_e32 v[96:97], v98
	v_cvt_pk_f32_fp8_sdwa v[98:99], v98 src0_sel:WORD_1
	s_waitcnt vmcnt(22)
	v_cvt_pk_f32_fp8_e32 v[100:101], v102
	v_cvt_pk_f32_fp8_sdwa v[102:103], v102 src0_sel:WORD_1
	v_cvt_pk_f32_fp8_e32 v[80:81], v82
	v_cvt_pk_f32_fp8_sdwa v[82:83], v82 src0_sel:WORD_1
	v_cvt_pk_f32_fp8_e32 v[84:85], v86
	v_cvt_pk_f32_fp8_sdwa v[86:87], v86 src0_sel:WORD_1
	v_cvt_pk_f32_fp8_e32 v[88:89], v90
	v_cvt_pk_f32_fp8_sdwa v[90:91], v90 src0_sel:WORD_1
	v_cvt_pk_f32_fp8_e32 v[92:93], v94
	v_cvt_pk_f32_fp8_sdwa v[94:95], v94 src0_sel:WORD_1
	s_waitcnt vmcnt(21)
	v_cvt_pk_f32_fp8_e32 v[104:105], v106
	v_cvt_pk_f32_fp8_sdwa v[106:107], v106 src0_sel:WORD_1
	s_waitcnt vmcnt(15)
	v_cvt_pk_f32_fp8_e32 v[128:129], v130
	v_cvt_pk_f32_fp8_sdwa v[130:131], v130 src0_sel:WORD_1
	s_waitcnt vmcnt(14)
	v_cvt_pk_f32_fp8_e32 v[132:133], v134
	v_cvt_pk_f32_fp8_sdwa v[134:135], v134 src0_sel:WORD_1
	v_cvt_pk_f32_fp8_e32 v[108:109], v110
	v_cvt_pk_f32_fp8_sdwa v[110:111], v110 src0_sel:WORD_1
	v_cvt_pk_f32_fp8_e32 v[112:113], v114
	v_cvt_pk_f32_fp8_sdwa v[114:115], v114 src0_sel:WORD_1
	v_cvt_pk_f32_fp8_e32 v[116:117], v118
	v_cvt_pk_f32_fp8_sdwa v[118:119], v118 src0_sel:WORD_1
	v_cvt_pk_f32_fp8_e32 v[120:121], v122
	v_cvt_pk_f32_fp8_sdwa v[122:123], v122 src0_sel:WORD_1
	v_cvt_pk_f32_fp8_e32 v[124:125], v126
	v_cvt_pk_f32_fp8_sdwa v[126:127], v126 src0_sel:WORD_1
	s_waitcnt vmcnt(13)
	v_cvt_pk_f32_fp8_e32 v[136:137], v138
	v_cvt_pk_f32_fp8_sdwa v[138:139], v138 src0_sel:WORD_1
	s_waitcnt vmcnt(7)
	v_cvt_pk_f32_fp8_e32 v[160:161], v162
	v_cvt_pk_f32_fp8_sdwa v[162:163], v162 src0_sel:WORD_1
	s_waitcnt vmcnt(6)
; __device__ __forceinline__ void p9_final(Ctx& X) {
;     ...
;             for (int j = 0; j < 8; ++j) { const int y = (int)yr[64 * j]; const f32x2 lo = __builtin_amdgcn_cvt_pk_f32_fp8(y, false), hi = __builtin_amdgcn_cvt_pk_f32_fp8(y, true);
;                 v[j].x += wk * lo.x; v[j].y += wk * lo.y; v[j].z += wk * hi.x; v[j].w += wk * hi.y; } }
	v_cvt_pk_f32_fp8_e32 v[164:165], v166
	v_cvt_pk_f32_fp8_sdwa v[166:167], v166 src0_sel:WORD_1
	v_cvt_pk_f32_fp8_e32 v[140:141], v142
	v_cvt_pk_f32_fp8_sdwa v[142:143], v142 src0_sel:WORD_1
	v_cvt_pk_f32_fp8_e32 v[144:145], v146
	v_cvt_pk_f32_fp8_sdwa v[146:147], v146 src0_sel:WORD_1
	v_cvt_pk_f32_fp8_e32 v[148:149], v150
	v_cvt_pk_f32_fp8_sdwa v[150:151], v150 src0_sel:WORD_1
	v_cvt_pk_f32_fp8_e32 v[152:153], v154
	v_cvt_pk_f32_fp8_sdwa v[154:155], v154 src0_sel:WORD_1
	v_cvt_pk_f32_fp8_e32 v[156:157], v158
	v_cvt_pk_f32_fp8_sdwa v[158:159], v158 src0_sel:WORD_1
	s_waitcnt vmcnt(5)
	v_cvt_pk_f32_fp8_e32 v[168:169], v170
	v_cvt_pk_f32_fp8_sdwa v[170:171], v170 src0_sel:WORD_1
	v_pk_fma_f32 v[32:33], v[28:29], v[56:57], v[32:33] op_sel_hi:[0,1,1]
	v_pk_fma_f32 v[36:37], v[28:29], v[58:59], v[36:37] op_sel_hi:[0,1,1]
	v_pk_fma_f32 v[38:39], v[28:29], v[60:61], v[38:39] op_sel_hi:[0,1,1]
	v_pk_fma_f32 v[40:41], v[28:29], v[62:63], v[40:41] op_sel_hi:[0,1,1]
	s_waitcnt vmcnt(4)
	v_cvt_pk_f32_fp8_e32 v[172:173], v174
	v_cvt_pk_f32_fp8_sdwa v[174:175], v174 src0_sel:WORD_1
	s_waitcnt vmcnt(3)
	v_cvt_pk_f32_fp8_e32 v[176:177], v178
	v_cvt_pk_f32_fp8_sdwa v[178:179], v178 src0_sel:WORD_1
	s_waitcnt vmcnt(2)
	v_cvt_pk_f32_fp8_e32 v[180:181], v182
	v_cvt_pk_f32_fp8_sdwa v[182:183], v182 src0_sel:WORD_1
	s_waitcnt vmcnt(1)
	v_cvt_pk_f32_fp8_e32 v[184:185], v186
	v_cvt_pk_f32_fp8_sdwa v[186:187], v186 src0_sel:WORD_1
	s_waitcnt vmcnt(0)
	v_cvt_pk_f32_fp8_e32 v[188:189], v190
	v_cvt_pk_f32_fp8_sdwa v[190:191], v190 src0_sel:WORD_1
	v_pk_fma_f32 v[44:45], v[28:29], v[64:65], v[44:45] op_sel_hi:[0,1,1]
	v_pk_fma_f32 v[42:43], v[28:29], v[74:75], v[42:43] op_sel_hi:[0,1,1]
	v_pk_fma_f32 v[32:33], v[4:5], v[96:97], v[32:33] op_sel_hi:[0,1,1]
	v_pk_fma_f32 v[36:37], v[4:5], v[98:99], v[36:37] op_sel_hi:[0,1,1]
	v_pk_fma_f32 v[38:39], v[4:5], v[100:101], v[38:39] op_sel_hi:[0,1,1]
	v_pk_fma_f32 v[40:41], v[4:5], v[102:103], v[40:41] op_sel_hi:[0,1,1]
	v_pk_fma_f32 v[46:47], v[28:29], v[76:77], v[46:47] op_sel_hi:[0,1,1]
	v_pk_fma_f32 v[34:35], v[28:29], v[78:79], v[34:35] op_sel_hi:[0,1,1]
	v_pk_fma_f32 v[56:57], v[28:29], v[80:81], v[66:67] op_sel_hi:[0,1,1]
	v_pk_fma_f32 v[30:31], v[28:29], v[82:83], v[30:31] op_sel_hi:[0,1,1]
	v_pk_fma_f32 v[58:59], v[28:29], v[84:85], v[68:69] op_sel_hi:[0,1,1]
	v_pk_fma_f32 v[26:27], v[28:29], v[86:87], v[26:27] op_sel_hi:[0,1,1]
	v_pk_fma_f32 v[60:61], v[28:29], v[88:89], v[70:71] op_sel_hi:[0,1,1]
	v_pk_fma_f32 v[22:23], v[28:29], v[90:91], v[22:23] op_sel_hi:[0,1,1]
	v_pk_fma_f32 v[62:63], v[28:29], v[92:93], v[72:73] op_sel_hi:[0,1,1]
	v_pk_fma_f32 v[20:21], v[28:29], v[94:95], v[20:21] op_sel_hi:[0,1,1]
	v_pk_fma_f32 v[44:45], v[4:5], v[104:105], v[44:45] op_sel_hi:[0,1,1]
	v_pk_fma_f32 v[42:43], v[4:5], v[106:107], v[42:43] op_sel_hi:[0,1,1]
	v_pk_fma_f32 v[32:33], v[24:25], v[128:129], v[32:33] op_sel_hi:[0,1,1]
	v_pk_fma_f32 v[36:37], v[24:25], v[130:131], v[36:37] op_sel_hi:[0,1,1]
	v_pk_fma_f32 v[38:39], v[24:25], v[132:133], v[38:39] op_sel_hi:[0,1,1]
	v_pk_fma_f32 v[40:41], v[24:25], v[134:135], v[40:41] op_sel_hi:[0,1,1]
	v_pk_fma_f32 v[46:47], v[4:5], v[108:109], v[46:47] op_sel_hi:[0,1,1]
	v_pk_fma_f32 v[34:35], v[4:5], v[110:111], v[34:35] op_sel_hi:[0,1,1]
	v_pk_fma_f32 v[56:57], v[4:5], v[112:113], v[56:57] op_sel_hi:[0,1,1]
	v_pk_fma_f32 v[30:31], v[4:5], v[114:115], v[30:31] op_sel_hi:[0,1,1]
	v_pk_fma_f32 v[58:59], v[4:5], v[116:117], v[58:59] op_sel_hi:[0,1,1]
	v_pk_fma_f32 v[26:27], v[4:5], v[118:119], v[26:27] op_sel_hi:[0,1,1]
	v_pk_fma_f32 v[60:61], v[4:5], v[120:121], v[60:61] op_sel_hi:[0,1,1]
	v_pk_fma_f32 v[22:23], v[4:5], v[122:123], v[22:23] op_sel_hi:[0,1,1]
	v_pk_fma_f32 v[62:63], v[4:5], v[124:125], v[62:63] op_sel_hi:[0,1,1]
	v_pk_fma_f32 v[20:21], v[4:5], v[126:127], v[20:21] op_sel_hi:[0,1,1]
	v_pk_fma_f32 v[44:45], v[24:25], v[136:137], v[44:45] op_sel_hi:[0,1,1]
	v_pk_fma_f32 v[42:43], v[24:25], v[138:139], v[42:43] op_sel_hi:[0,1,1]
	v_pk_fma_f32 v[32:33], v[24:25], v[160:161], v[32:33] op_sel:[1,0,0]
	v_pk_fma_f32 v[36:37], v[24:25], v[162:163], v[36:37] op_sel:[1,0,0]
	v_pk_fma_f32 v[38:39], v[24:25], v[164:165], v[38:39] op_sel:[1,0,0]
	v_pk_fma_f32 v[40:41], v[24:25], v[166:167], v[40:41] op_sel:[1,0,0]
	v_pk_fma_f32 v[46:47], v[24:25], v[140:141], v[46:47] op_sel_hi:[0,1,1]
	v_pk_fma_f32 v[34:35], v[24:25], v[142:143], v[34:35] op_sel_hi:[0,1,1]
	v_pk_fma_f32 v[56:57], v[24:25], v[144:145], v[56:57] op_sel_hi:[0,1,1]
	v_pk_fma_f32 v[30:31], v[24:25], v[146:147], v[30:31] op_sel_hi:[0,1,1]
	v_pk_fma_f32 v[58:59], v[24:25], v[148:149], v[58:59] op_sel_hi:[0,1,1]
	v_pk_fma_f32 v[26:27], v[24:25], v[150:151], v[26:27] op_sel_hi:[0,1,1]
	v_pk_fma_f32 v[60:61], v[24:25], v[152:153], v[60:61] op_sel_hi:[0,1,1]
	v_pk_fma_f32 v[22:23], v[24:25], v[154:155], v[22:23] op_sel_hi:[0,1,1]
	v_pk_fma_f32 v[62:63], v[24:25], v[156:157], v[62:63] op_sel_hi:[0,1,1]
	v_pk_fma_f32 v[20:21], v[24:25], v[158:159], v[20:21] op_sel_hi:[0,1,1]
	v_pk_fma_f32 v[44:45], v[24:25], v[168:169], v[44:45] op_sel:[1,0,0]
	v_pk_fma_f32 v[42:43], v[24:25], v[170:171], v[42:43] op_sel:[1,0,0]
	v_mov_b32_e32 v64, v33
	v_mov_b32_e32 v65, v39
	v_mov_b32_e32 v68, v37
	v_mov_b32_e32 v69, v41
	v_pk_fma_f32 v[46:47], v[24:25], v[172:173], v[46:47] op_sel:[1,0,0]
	v_pk_fma_f32 v[34:35], v[24:25], v[174:175], v[34:35] op_sel:[1,0,0]
	v_pk_fma_f32 v[56:57], v[24:25], v[176:177], v[56:57] op_sel:[1,0,0]
	v_pk_fma_f32 v[30:31], v[24:25], v[178:179], v[30:31] op_sel:[1,0,0]
; __device__ __forceinline__ void p9_final(Ctx& X) {
;     ...
;         float s = 0.f;
; #pragma unroll
;         for (int j = 0; j < 8; ++j) s += (v[j].x * v[j].x + v[j].y * v[j].y) + (v[j].z * v[j].z + v[j].w * v[j].w);
;         const float rstd = rsqrtf(wave_sum(s) * (1.f / D) + EPS);
;         f32x4* o = (f32x4*)(X.out + (size_t)t * D) + lane; const f32x4* wr_ = (const f32x4*)XP_ln_final_w(X) + lane;
; #pragma unroll
;         for (int j = 0; j < 8; ++j) { const f32x4 wv = wr_[64 * j]; f32x4 r; r.x = v[j].x * rstd * wv.x; r.y = v[j].y * rstd * wv.y; r.z = v[j].z * rstd * wv.z; r.w = v[j].w * rstd * wv.w; __builtin_nontemporal_store(r, &o[64 * j]); }
	v_pk_fma_f32 v[58:59], v[24:25], v[180:181], v[58:59] op_sel:[1,0,0]
	v_pk_fma_f32 v[26:27], v[24:25], v[182:183], v[26:27] op_sel:[1,0,0]
	v_pk_fma_f32 v[60:61], v[24:25], v[184:185], v[60:61] op_sel:[1,0,0]
	v_pk_fma_f32 v[22:23], v[24:25], v[186:187], v[22:23] op_sel:[1,0,0]
	v_pk_fma_f32 v[62:63], v[24:25], v[188:189], v[62:63] op_sel:[1,0,0]
	v_pk_fma_f32 v[20:21], v[24:25], v[190:191], v[20:21] op_sel:[1,0,0]
	v_mov_b32_e32 v24, v32
	v_mov_b32_e32 v25, v38
	v_mov_b32_e32 v66, v36
	v_mov_b32_e32 v67, v40
	v_mov_b32_e32 v72, v45
	v_mov_b32_e32 v73, v43
	v_pk_mul_f32 v[64:65], v[64:65], v[64:65]
	v_pk_mul_f32 v[68:69], v[68:69], v[68:69]
	v_mov_b32_e32 v70, v44
	v_mov_b32_e32 v71, v42
	v_pk_mul_f32 v[72:73], v[72:73], v[72:73]
	v_pk_fma_f32 v[24:25], v[24:25], v[24:25], v[64:65]
	v_pk_fma_f32 v[64:65], v[66:67], v[66:67], v[68:69]
	v_mul_f32_e32 v4, v47, v47
	v_mul_f32_e32 v28, v35, v35
	v_pk_fma_f32 v[66:67], v[70:71], v[70:71], v[72:73]
	v_pk_add_f32 v[24:25], v[24:25], v[64:65]
	v_pk_mul_f32 v[74:75], v[56:57], v[56:57]
	v_pk_mul_f32 v[76:77], v[30:31], v[30:31]
	v_pk_fma_f32 v[90:91], v[46:47], v[46:47], v[4:5] op_sel_hi:[1,1,0]
	v_pk_fma_f32 v[92:93], v[34:35], v[34:35], v[28:29] op_sel_hi:[1,1,0]
	v_pk_add_f32 v[64:65], v[66:67], v[66:67] op_sel:[0,1] op_sel_hi:[1,0]
	v_pk_add_f32 v[24:25], v[24:25], v[24:25] op_sel:[0,1] op_sel_hi:[1,0]
	v_mov_b32_e32 v80, v59
	v_mov_b32_e32 v81, v27
	v_mov_b32_e32 v91, v76
	v_mov_b32_e32 v93, v77
	v_mov_b32_e32 v65, v75
	v_mov_b32_e32 v25, v74
	v_mov_b32_e32 v78, v58
	v_mov_b32_e32 v79, v26
	v_pk_mul_f32 v[80:81], v[80:81], v[80:81]
	v_pk_add_f32 v[66:67], v[90:91], v[92:93]
	v_pk_add_f32 v[24:25], v[24:25], v[64:65]
	v_mul_f32_e32 v82, v61, v61
	v_mul_f32_e32 v84, v23, v23
	v_pk_fma_f32 v[68:69], v[78:79], v[78:79], v[80:81]
	v_pk_add_f32 v[24:25], v[24:25], v[66:67]
	v_pk_mul_f32 v[86:87], v[62:63], v[62:63]
	v_pk_mul_f32 v[88:89], v[20:21], v[20:21]
	v_pk_fma_f32 v[82:83], v[60:61], v[60:61], v[82:83] op_sel_hi:[1,1,0]
	v_pk_fma_f32 v[84:85], v[22:23], v[22:23], v[84:85] op_sel_hi:[1,1,0]
	v_pk_add_f32 v[68:69], v[68:69], v[68:69] op_sel:[0,1] op_sel_hi:[1,0]
	v_pk_add_f32 v[24:25], v[24:25], v[24:25] op_sel:[0,1] op_sel_hi:[1,0]
	v_mov_b32_e32 v83, v88
	v_mov_b32_e32 v85, v89
	v_mov_b32_e32 v69, v87
	v_mov_b32_e32 v25, v86
	v_pk_add_f32 v[70:71], v[82:83], v[84:85]
	v_pk_add_f32 v[24:25], v[24:25], v[68:69]
	s_nop 0
	v_pk_add_f32 v[24:25], v[24:25], v[70:71]
	s_nop 0
	v_add_f32_e32 v4, v24, v25
	ds_bpermute_b32 v24, v29, v4
	s_waitcnt lgkmcnt(0)
	v_add_f32_e32 v4, v4, v24
	ds_bpermute_b32 v24, v48, v4
	s_waitcnt lgkmcnt(0)
	v_add_f32_e32 v4, v4, v24
	ds_bpermute_b32 v24, v49, v4
	s_waitcnt lgkmcnt(0)
	v_add_f32_e32 v4, v4, v24
	ds_bpermute_b32 v24, v50, v4
	s_waitcnt lgkmcnt(0)
	v_add_f32_e32 v4, v4, v24
	ds_bpermute_b32 v24, v51, v4
	s_waitcnt lgkmcnt(0)
	v_add_f32_e32 v4, v4, v24
	ds_bpermute_b32 v24, v52, v4
	s_waitcnt lgkmcnt(0)
	v_add_f32_e32 v4, v4, v24
	v_fmamk_f32 v4, v4, 0x3a000000, v54
	v_mul_f32_e32 v24, 0x4b800000, v4
	v_cmp_gt_f32_e32 vcc, s5, v4
	s_nop 1
	v_cndmask_b32_e32 v4, v4, v24, vcc
	v_rsq_f32_e32 v4, v4
	s_nop 0
	v_mul_f32_e32 v24, 0x45800000, v4
	v_cndmask_b32_e32 v4, v4, v24, vcc
	v_pk_mul_f32 v[24:25], v[32:33], v[4:5] op_sel_hi:[1,0]
	v_pk_mul_f32 v[32:33], v[36:37], v[4:5] op_sel_hi:[1,0]
	v_pk_mul_f32 v[228:229], v[196:197], v[24:25]
	v_pk_mul_f32 v[230:231], v[198:199], v[32:33]
	global_store_dwordx4 v[18:19], v[228:231], off offset:-4096 nt
	v_pk_mul_f32 v[24:25], v[40:41], v[4:5] op_sel_hi:[1,0]
	v_pk_mul_f32 v[32:33], v[38:39], v[4:5] op_sel_hi:[1,0]
	v_pk_mul_f32 v[22:23], v[22:23], v[4:5] op_sel_hi:[1,0]
	v_pk_mul_f32 v[20:21], v[20:21], v[4:5] op_sel_hi:[1,0]
	v_pk_mul_f32 v[232:233], v[200:201], v[32:33]
	v_pk_mul_f32 v[234:235], v[202:203], v[24:25]
	global_store_dwordx4 v[18:19], v[232:235], off offset:-3072 nt
	v_pk_mul_f32 v[24:25], v[42:43], v[4:5] op_sel_hi:[1,0]
	v_pk_mul_f32 v[32:33], v[44:45], v[4:5] op_sel_hi:[1,0]
	v_pk_mul_f32 v[230:231], v[206:207], v[24:25]
	v_pk_mul_f32 v[228:229], v[204:205], v[32:33]
	global_store_dwordx4 v[18:19], v[228:231], off offset:-2048 nt
	v_pk_mul_f32 v[24:25], v[34:35], v[4:5] op_sel_hi:[1,0]
	v_pk_mul_f32 v[32:33], v[46:47], v[4:5] op_sel_hi:[1,0]
	v_pk_mul_f32 v[234:235], v[210:211], v[24:25]
	v_pk_mul_f32 v[232:233], v[208:209], v[32:33]
	global_store_dwordx4 v[18:19], v[232:235], off offset:-1024 nt
	v_pk_mul_f32 v[24:25], v[30:31], v[4:5] op_sel_hi:[1,0]
	v_pk_mul_f32 v[30:31], v[56:57], v[4:5] op_sel_hi:[1,0]
	v_pk_mul_f32 v[230:231], v[214:215], v[24:25]
	v_pk_mul_f32 v[228:229], v[212:213], v[30:31]
	global_store_dwordx4 v[18:19], v[228:231], off nt
	v_pk_mul_f32 v[24:25], v[26:27], v[4:5] op_sel_hi:[1,0]
	v_pk_mul_f32 v[26:27], v[58:59], v[4:5] op_sel_hi:[1,0]
	v_pk_mul_f32 v[234:235], v[218:219], v[24:25]
	v_pk_mul_f32 v[232:233], v[216:217], v[26:27]
	global_store_dwordx4 v[18:19], v[232:235], off offset:1024 nt
	v_pk_mul_f32 v[24:25], v[60:61], v[4:5] op_sel_hi:[1,0]
	v_pk_mul_f32 v[230:231], v[22:23], v[222:223]
	v_pk_mul_f32 v[228:229], v[24:25], v[220:221]
	global_store_dwordx4 v[18:19], v[228:231], off offset:2048 nt
	v_pk_mul_f32 v[22:23], v[62:63], v[4:5] op_sel_hi:[1,0]
	v_pk_mul_f32 v[234:235], v[20:21], v[226:227]
	v_pk_mul_f32 v[232:233], v[22:23], v[224:225]
	global_store_dwordx4 v[18:19], v[232:235], off offset:3072 nt
	v_lshl_add_u64 v[18:19], v[18:19], 0, s[10:11]
	s_cbranch_scc1 .LBB0_1128
